# baseline (speedup 1.0000x reference)
_Z12k_recon_mfmaPKDF16_PKDv8_DF16_PKfPf:
	s_load_dwordx4 s[4:7], s[0:1], 0x0
	s_load_dwordx2 s[8:9], s[0:1], 0x10
	v_readfirstlane_b32 s13, v0
	s_lshr_b32 s3, s2, 4
	s_mul_i32 s12, s3, 0x640
	v_add_u32_e32 v30, s12, v0
	v_mov_b32_e32 v31, 0
	s_lshl_b32 s13, s13, 4
	s_waitcnt lgkmcnt(0)
	v_lshl_add_u64 v[2:3], v[30:31], 4, s[6:7]
	s_mov_b32 m0, s13
	s_nop 0
	global_load_lds_dwordx4 v[2:3], off
	s_movk_i32 s10, 0x640
	v_or_b32_e32 v1, 0x400, v0
	v_cmp_gt_u32_e32 vcc, s10, v1
	s_and_saveexec_b64 s[10:11], vcc
	s_cbranch_execz .LBB1_2
	v_add_u32_e32 v30, s12, v1
	v_lshl_add_u64 v[2:3], v[30:31], 4, s[6:7]
	s_add_u32 m0, s13, 0x4000
	s_nop 0
	global_load_lds_dwordx4 v[2:3], off
.LBB1_2:
	s_or_b64 exec, exec, s[10:11]
	s_lshl_b32 s7, s2, 1
	s_bfe_u32 s2, s2, 0x10003
	v_readfirstlane_b32 s6, v0
	s_and_b32 s7, s7, 14
	s_or_b32 s7, s7, s2
	s_lshr_b32 s10, s6, 2
	s_lshl_b32 s2, s7, 8
	s_and_b32 s10, s10, 0x3ffffff0
	v_and_b32_e32 v1, 15, v0
	s_add_i32 s10, s10, s2
	v_or_b32_e32 v4, s10, v1
	s_movk_i32 s2, 0x140
	v_mov_b64_e32 v[2:3], s[4:5]
	v_mad_u64_u32 v[2:3], s[4:5], v4, s2, v[2:3]
	v_and_b32_e32 v30, 48, v0
	v_lshl_add_u64 v[32:33], v[2:3], 0, v[30:31]
	s_mul_i32 s3, s3, 10
	v_bfe_u32 v30, v0, 5, 1
	v_or_b32_e32 v30, s3, v30
	v_lshl_add_u64 v[42:43], v[30:31], 2, s[8:9]
	global_load_dwordx4 v[18:21], v[32:33], off
	global_load_dwordx4 v[14:17], v[32:33], off offset:64
	global_load_dwordx4 v[10:13], v[32:33], off offset:128
	global_load_dwordx4 v[6:9], v[32:33], off offset:192
	global_load_dwordx4 v[2:5], v[32:33], off offset:256
	global_load_dword v40, v[42:43], off
	global_load_dword v38, v[42:43], off offset:8
	global_load_dword v36, v[42:43], off offset:16
	global_load_dword v34, v[42:43], off offset:24
	s_nop 0
	global_load_dword v32, v[42:43], off offset:32
	s_load_dwordx2 s[0:1], s[0:1], 0x18
	v_and_b32_e32 v35, 63, v0
	v_bfe_u32 v33, v0, 4, 2
	v_lshlrev_b32_e32 v0, 4, v0
	s_waitcnt vmcnt(10)
	v_lshlrev_b32_e32 v35, 4, v35
	s_waitcnt lgkmcnt(0)
	s_barrier
	ds_read_b128 v[22:25], v35
	ds_read_b128 v[26:29], v35 offset:1024
	ds_read_b128 v[46:49], v35 offset:2048
	s_waitcnt vmcnt(9) lgkmcnt(2)
	v_mfma_f32_16x16x32_f16 v[22:25], v[22:25], v[18:21], 0
	ds_read_b128 v[42:45], v35 offset:5120
	ds_read_b128 v[50:53], v35 offset:8192
	v_lshlrev_b32_e32 v0, 12, v33
	s_waitcnt vmcnt(8) lgkmcnt(3)
	v_mfma_f32_16x16x32_f16 v[22:25], v[26:29], v[14:17], v[22:25]
	ds_read_b128 v[26:29], v35 offset:3072
	v_mov_b32_e32 v55, 0
	v_and_b32_e32 v0, 0x1000, v0
	s_waitcnt vmcnt(7) lgkmcnt(3)
	v_mfma_f32_16x16x32_f16 v[22:25], v[46:49], v[10:13], v[22:25]
	ds_read_b128 v[46:49], v35 offset:4096
	v_lshl_or_b32 v58, s7, 13, v0
	v_mov_b32_e32 v59, v55
	s_waitcnt vmcnt(6) lgkmcnt(1)
	v_mfma_f32_16x16x32_f16 v[22:25], v[26:29], v[6:9], v[22:25]
	ds_read_b128 v[26:29], v35 offset:6144
	v_lshlrev_b32_e32 v0, 3, v1
	v_and_b32_e32 v64, 1, v1
	s_movk_i32 s18, 0x78
	v_mad_u32_u24 v0, v64, s18, v0
	s_mov_b32 s14, 0x55555555
	s_mov_b32 s15, 0x55555555
	s_not_b64 s[16:17], s[14:15]
	v_mov_b32_e32 v1, v55
	s_waitcnt vmcnt(5) lgkmcnt(1)
	v_mfma_f32_16x16x32_f16 v[22:25], v[46:49], v[2:5], v[22:25]
	ds_read_b128 v[46:49], v35 offset:7168
	v_add_u32_e32 v54, 2, v30
	v_add_u32_e32 v56, 4, v30
	v_mfma_f32_16x16x32_f16 v[42:45], v[42:45], v[18:21], 0
	v_mov_b32_e32 v57, v55
	s_waitcnt vmcnt(4)
	s_nop 1
	v_pk_add_f32 v[60:61], v[22:23], v[40:41] op_sel_hi:[1,0]
	v_pk_add_f32 v[62:63], v[24:25], v[40:41] op_sel_hi:[1,0]
	s_waitcnt lgkmcnt(1)
	v_mfma_f32_16x16x32_f16 v[26:29], v[26:29], v[14:17], v[42:45]
	s_waitcnt lgkmcnt(0)
	v_mfma_f32_16x16x32_f16 v[26:29], v[46:49], v[10:13], v[26:29]
	s_nop 0
	ds_read_b128 v[42:45], v35 offset:9216
	ds_read_b128 v[46:49], v35 offset:10240
	v_mfma_f32_16x16x32_f16 v[26:29], v[50:53], v[6:9], v[26:29]
	ds_read_b128 v[50:53], v35 offset:11264
	s_waitcnt lgkmcnt(2)
	v_mfma_f32_16x16x32_f16 v[26:29], v[42:45], v[2:5], v[26:29]
	ds_read_b128 v[40:43], v35 offset:12288
	s_waitcnt lgkmcnt(2)
	v_mfma_f32_16x16x32_f16 v[22:25], v[46:49], v[18:21], 0
	ds_read_b128 v[44:47], v35 offset:13312
	v_lshl_add_u64 v[48:49], s[0:1], 0, v[58:59]
	s_and_b32 s0, s6, 0xffffffc0
	s_waitcnt lgkmcnt(2)
	v_mfma_f32_16x16x32_f16 v[22:25], v[50:53], v[14:17], v[22:25]
	s_ashr_i32 s1, s0, 31
	v_lshl_add_u64 v[48:49], s[0:1], 2, v[48:49]
	v_lshl_add_u64 v[0:1], v[48:49], 0, v[0:1]
	s_waitcnt lgkmcnt(1)
	v_mfma_f32_16x16x32_f16 v[22:25], v[40:43], v[10:13], v[22:25]
	ds_read_b128 v[40:43], v35 offset:14336
	v_lshlrev_b64 v[48:49], 17, v[30:31]
	v_lshl_add_u64 v[48:49], v[0:1], 0, v[48:49]
	s_waitcnt lgkmcnt(1)
	v_mfma_f32_16x16x32_f16 v[22:25], v[44:47], v[6:9], v[22:25]
	ds_read_b128 v[44:47], v35 offset:15360
	s_mov_b64 vcc, s[14:15]
	v_cndmask_b32_dpp v64, v62, v60, vcc quad_perm:[1,0,3,2] row_mask:0xf bank_mask:0xf
	v_cndmask_b32_dpp v65, v63, v61, vcc quad_perm:[1,0,3,2] row_mask:0xf bank_mask:0xf
	s_mov_b64 vcc, s[16:17]
	v_cndmask_b32_dpp v66, v60, v62, vcc quad_perm:[1,0,3,2] row_mask:0xf bank_mask:0xf
	v_cndmask_b32_dpp v67, v61, v63, vcc quad_perm:[1,0,3,2] row_mask:0xf bank_mask:0xf
	global_store_dwordx4 v[48:49], v[64:67], off sc1
	ds_read_b128 v[48:51], v35 offset:16384
	s_waitcnt vmcnt(4)
	v_pk_add_f32 v[52:53], v[26:27], v[38:39] op_sel_hi:[1,0]
	v_pk_add_f32 v[58:59], v[28:29], v[38:39] op_sel_hi:[1,0]
	ds_read_b128 v[26:29], v35 offset:17408
	s_waitcnt lgkmcnt(3)
	v_mfma_f32_16x16x32_f16 v[22:25], v[40:43], v[2:5], v[22:25]
	v_add_u32_e32 v60, 6, v30
	v_mov_b32_e32 v61, v55
	v_add_u32_e32 v30, 8, v30
	s_waitcnt lgkmcnt(2)
	v_mfma_f32_16x16x32_f16 v[38:41], v[44:47], v[18:21], 0
	ds_read_b128 v[42:45], v35 offset:18432
	v_lshlrev_b64 v[46:47], 17, v[54:55]
	v_lshl_add_u64 v[46:47], v[0:1], 0, v[46:47]
	s_waitcnt lgkmcnt(2)
	v_mfma_f32_16x16x32_f16 v[38:41], v[48:51], v[14:17], v[38:41]
	v_mov_b32_e32 v31, v55
	s_waitcnt lgkmcnt(1)
	v_mfma_f32_16x16x32_f16 v[26:29], v[26:29], v[10:13], v[38:41]
	s_nop 4
	ds_read_b128 v[38:41], v35 offset:19456
	s_mov_b64 vcc, s[14:15]
	v_cndmask_b32_dpp v68, v58, v52, vcc quad_perm:[1,0,3,2] row_mask:0xf bank_mask:0xf
	v_cndmask_b32_dpp v69, v59, v53, vcc quad_perm:[1,0,3,2] row_mask:0xf bank_mask:0xf
	s_mov_b64 vcc, s[16:17]
	v_cndmask_b32_dpp v70, v52, v58, vcc quad_perm:[1,0,3,2] row_mask:0xf bank_mask:0xf
	v_cndmask_b32_dpp v71, v53, v59, vcc quad_perm:[1,0,3,2] row_mask:0xf bank_mask:0xf
	global_store_dwordx4 v[46:47], v[68:71], off sc1
	ds_read_b128 v[46:49], v35 offset:20480
	s_waitcnt lgkmcnt(2)
	v_mfma_f32_16x16x32_f16 v[26:29], v[42:45], v[6:9], v[26:29]
	v_lshlrev_b64 v[42:43], 17, v[56:57]
	v_lshl_add_u64 v[50:51], v[0:1], 0, v[42:43]
	ds_read_b128 v[42:45], v35 offset:21504
	s_waitcnt lgkmcnt(2)
	v_mfma_f32_16x16x32_f16 v[26:29], v[38:41], v[2:5], v[26:29]
	s_waitcnt vmcnt(4)
	v_pk_add_f32 v[38:39], v[22:23], v[36:37] op_sel_hi:[1,0]
	v_pk_add_f32 v[36:37], v[24:25], v[36:37] op_sel_hi:[1,0]
	ds_read_b128 v[22:25], v35 offset:22528
	s_waitcnt lgkmcnt(2)
	v_mfma_f32_16x16x32_f16 v[18:21], v[46:49], v[18:21], 0
	s_mov_b64 vcc, s[14:15]
	v_cndmask_b32_dpp v72, v36, v38, vcc quad_perm:[1,0,3,2] row_mask:0xf bank_mask:0xf
	v_cndmask_b32_dpp v73, v37, v39, vcc quad_perm:[1,0,3,2] row_mask:0xf bank_mask:0xf
	s_mov_b64 vcc, s[16:17]
	v_cndmask_b32_dpp v74, v38, v36, vcc quad_perm:[1,0,3,2] row_mask:0xf bank_mask:0xf
	v_cndmask_b32_dpp v75, v39, v37, vcc quad_perm:[1,0,3,2] row_mask:0xf bank_mask:0xf
	global_store_dwordx4 v[50:51], v[72:75], off sc1
	ds_read_b128 v[36:39], v35 offset:23552
	s_waitcnt lgkmcnt(2)
	v_mfma_f32_16x16x32_f16 v[14:17], v[42:45], v[14:17], v[18:21]
	s_nop 2
	v_lshlrev_b64 v[18:19], 17, v[60:61]
	v_lshl_add_u64 v[40:41], v[0:1], 0, v[18:19]
	ds_read_b128 v[18:21], v35 offset:24576
	s_waitcnt lgkmcnt(2)
	v_mfma_f32_16x16x32_f16 v[10:13], v[22:25], v[10:13], v[14:17]
	s_waitcnt lgkmcnt(1)
	v_mfma_f32_16x16x32_f16 v[6:9], v[36:39], v[6:9], v[10:13]
	s_waitcnt vmcnt(4)
	v_pk_add_f32 v[14:15], v[26:27], v[34:35] op_sel_hi:[1,0]
	v_pk_add_f32 v[16:17], v[28:29], v[34:35] op_sel_hi:[1,0]
	s_nop 1
	v_lshlrev_b64 v[10:11], 17, v[30:31]
	v_lshl_add_u64 v[10:11], v[0:1], 0, v[10:11]
	s_waitcnt lgkmcnt(0)
	v_mfma_f32_16x16x32_f16 v[0:3], v[18:21], v[2:5], v[6:9]
	s_mov_b64 vcc, s[14:15]
	v_cndmask_b32_dpp v76, v16, v14, vcc quad_perm:[1,0,3,2] row_mask:0xf bank_mask:0xf
	v_cndmask_b32_dpp v77, v17, v15, vcc quad_perm:[1,0,3,2] row_mask:0xf bank_mask:0xf
	s_mov_b64 vcc, s[16:17]
	v_cndmask_b32_dpp v78, v14, v16, vcc quad_perm:[1,0,3,2] row_mask:0xf bank_mask:0xf
	v_cndmask_b32_dpp v79, v15, v17, vcc quad_perm:[1,0,3,2] row_mask:0xf bank_mask:0xf
	global_store_dwordx4 v[40:41], v[76:79], off sc1
	s_waitcnt vmcnt(4)
	s_nop 5
	v_pk_add_f32 v[0:1], v[0:1], v[32:33] op_sel_hi:[1,0]
	v_pk_add_f32 v[2:3], v[2:3], v[32:33] op_sel_hi:[1,0]
	s_nop 1
	s_mov_b64 vcc, s[14:15]
	v_cndmask_b32_dpp v80, v2, v0, vcc quad_perm:[1,0,3,2] row_mask:0xf bank_mask:0xf
	v_cndmask_b32_dpp v81, v3, v1, vcc quad_perm:[1,0,3,2] row_mask:0xf bank_mask:0xf
	s_mov_b64 vcc, s[16:17]
	v_cndmask_b32_dpp v82, v0, v2, vcc quad_perm:[1,0,3,2] row_mask:0xf bank_mask:0xf
	v_cndmask_b32_dpp v83, v1, v3, vcc quad_perm:[1,0,3,2] row_mask:0xf bank_mask:0xf
	global_store_dwordx4 v[10:11], v[80:83], off sc1
	s_endpgm
